# attention loops: next-tile K/V LDS staging writes + global loads moved from the iteration head to behind the QK block (LDS write traffic overlaps the softmax VALU; QK fragment reads no longer queue be
# speedup vs baseline: 1.0121x; 1.0121x over previous
; #define SBAR() __builtin_amdgcn_sched_barrier(0)
; #define SLOAD(k0) do { vs0 = *reinterpret_cast<const bf16x8*>(Vh + (long)((k0) + sr) * DV + sc); vs1 = *reinterpret_cast<const bf16x8*>(Vh + (long)((k0) + 32 + sr) * DV + sc); \
;     const bf16_t* kp_ = Kh + (long)(k0) * QK + tid * 8; ks0 = *reinterpret_cast<const bf16x8*>(kp_); ks1 = *reinterpret_cast<const bf16x8*>(kp_ + 4096); ks2 = *reinterpret_cast<const bf16x8*>(kp_ + 8192); } while (0)
; #define SWRITE(b) do { *(bf16x8*)(V_lds + (b) * SHM_V + vst0) = vs0; *(bf16x8*)(V_lds + (b) * SHM_V + vst1) = vs1; \
;     *(bf16x8*)(K_lds + (b) * SHM_K + kst[0]) = ks0; *(bf16x8*)(K_lds + (b) * SHM_K + kst[1]) = ks1; *(bf16x8*)(K_lds + (b) * SHM_K + kst[2]) = ks2; } while (0)
; #define SWAIT() asm volatile("s_waitcnt vmcnt(0)" ::: "memory")
; DEV void attn_unit(const bf16_t* __restrict__ Qb, const bf16_t* __restrict__ Kh, const bf16_t* __restrict__ Vh, const float* __restrict__ rp, bf16_t* __restrict__ Ob, CParams& fp, int fwg, int fbase, int fn) {
;     ...
;   for (int j = 0; j < NTL; ++j) {
;     const int cb = j & 1;
;     if (j + 1 < NTL) { if (j >= 2 && j < fn) asm volatile("s_waitcnt vmcnt(5)" ::: "memory"); else SWAIT(); SWRITE(cb ^ 1); }
;     if (j + 2 < NTL) SLOAD((j + 2) * KVBLK);
;     if (j > 0 && j <= fn) fill_store(fp, fwg, fbase + j - 1, (j - 1) & 1);
;     SBAR(); qkt(p0, p1, K_lds + cb * SHM_K, qr, r32, hi);
.LBB0_891:
.LBB0_893:
.LBB0_892:
	s_add_i32 s35, s34, 1
	s_cmp_gt_u32 s35, 62
	s_cbranch_scc0 .LBB0_899
	s_branch .LBB0_907

; #define SBAR() __builtin_amdgcn_sched_barrier(0)
; DEV void qkt(f32x16& p0, f32x16& p1, const char* Ks, const bf16x8* qr, int r32, int hi) {
;   p0 = f32x16{}; p1 = f32x16{};
;   __builtin_amdgcn_s_setprio(1);
; #pragma unroll
;   for (int d0 = 0; d0 < 12; ++d0) { const int cb = (d0 * 16 + hi * 8) * 2;
;     const bf16x8 b0 = *reinterpret_cast<const bf16x8*>(Ks + KSWZ2(r32, cb));
;     const bf16x8 b1 = *reinterpret_cast<const bf16x8*>(Ks + KSWZ2(32 + r32, cb));
;     p0 = __builtin_amdgcn_mfma_f32_32x32x16_bf16(b0, qr[d0], p0, 0, 0, 0);
;     p1 = __builtin_amdgcn_mfma_f32_32x32x16_bf16(b1, qr[d0], p1, 0, 0, 0); }
;   __builtin_amdgcn_s_setprio(0);
; }
; DEV void attn_unit(const bf16_t* __restrict__ Qb, const bf16_t* __restrict__ Kh, const bf16_t* __restrict__ Vh, const float* __restrict__ rp, bf16_t* __restrict__ Ob, CParams& fp, int fwg, int fbase, int fn) {
;     ...
;     SBAR(); qkt(p0, p1, K_lds + cb * SHM_K, qr, r32, hi);
.Lfst_a_end:
.LBB0_907:
	s_lshl_b32 s6, s36, 15
	s_add_i32 s6, s6, 0
	s_setprio 1
	v_add3_u32 v66, s6, v201, v200
	ds_read_b128 v[68:71], v66 offset:32768
	ds_read_b128 v[72:75], v66 offset:49152
	v_add3_u32 v66, s6, v202, v200
	ds_read_b128 v[224:227], v66 offset:32768
	ds_read_b128 v[228:231], v66 offset:49152
	v_add3_u32 v66, s6, v203, v200
	s_waitcnt lgkmcnt(0)
	v_mfma_f32_32x32x16_bf16 v[84:99], v[68:71], v[100:103], 0
	v_mfma_f32_32x32x16_bf16 v[68:83], v[72:75], v[100:103], 0
	v_mfma_f32_32x32x16_bf16 v[84:99], v[224:227], v[104:107], v[84:99]
	v_mfma_f32_32x32x16_bf16 v[68:83], v[228:231], v[104:107], v[68:83]
	ds_read_b128 v[224:227], v66 offset:32768
	ds_read_b128 v[228:231], v66 offset:49152
	v_add3_u32 v66, s6, v204, v200
	s_waitcnt lgkmcnt(1)
	v_mfma_f32_32x32x16_bf16 v[84:99], v[224:227], v[108:111], v[84:99]
	s_waitcnt lgkmcnt(0)
	v_mfma_f32_32x32x16_bf16 v[68:83], v[228:231], v[108:111], v[68:83]
	ds_read_b128 v[224:227], v66 offset:32768
	ds_read_b128 v[228:231], v66 offset:49152
	v_add3_u32 v66, s6, v205, v200
	s_waitcnt lgkmcnt(1)
	v_mfma_f32_32x32x16_bf16 v[84:99], v[224:227], v[112:115], v[84:99]
	s_waitcnt lgkmcnt(0)
	v_mfma_f32_32x32x16_bf16 v[68:83], v[228:231], v[112:115], v[68:83]
	ds_read_b128 v[224:227], v66 offset:32768
	ds_read_b128 v[228:231], v66 offset:49152
	v_add3_u32 v66, s6, v206, v200
	s_waitcnt lgkmcnt(1)
	v_mfma_f32_32x32x16_bf16 v[84:99], v[224:227], v[116:119], v[84:99]
	s_waitcnt lgkmcnt(0)
	v_mfma_f32_32x32x16_bf16 v[68:83], v[228:231], v[116:119], v[68:83]
	ds_read_b128 v[224:227], v66 offset:32768
	ds_read_b128 v[228:231], v66 offset:49152
	v_add3_u32 v66, s6, v207, v200
	s_waitcnt lgkmcnt(1)
	v_mfma_f32_32x32x16_bf16 v[84:99], v[224:227], v[120:123], v[84:99]
	s_waitcnt lgkmcnt(0)
	v_mfma_f32_32x32x16_bf16 v[68:83], v[228:231], v[120:123], v[68:83]
	ds_read_b128 v[224:227], v66 offset:32768
	ds_read_b128 v[228:231], v66 offset:49152
	v_add3_u32 v66, s6, v208, v200
	s_waitcnt lgkmcnt(1)
	v_mfma_f32_32x32x16_bf16 v[84:99], v[224:227], v[124:127], v[84:99]
	s_waitcnt lgkmcnt(0)
	v_mfma_f32_32x32x16_bf16 v[68:83], v[228:231], v[124:127], v[68:83]
	ds_read_b128 v[224:227], v66 offset:32768
	ds_read_b128 v[228:231], v66 offset:49152
	v_add3_u32 v66, s6, v209, v200
	s_waitcnt lgkmcnt(1)
	v_mfma_f32_32x32x16_bf16 v[84:99], v[224:227], v[128:131], v[84:99]
	s_waitcnt lgkmcnt(0)
	v_mfma_f32_32x32x16_bf16 v[68:83], v[228:231], v[128:131], v[68:83]
	ds_read_b128 v[224:227], v66 offset:32768
	ds_read_b128 v[228:231], v66 offset:49152
	v_add3_u32 v66, s6, v211, v200
	s_waitcnt lgkmcnt(1)
	v_mfma_f32_32x32x16_bf16 v[84:99], v[224:227], v[132:135], v[84:99]
	s_waitcnt lgkmcnt(0)
	v_mfma_f32_32x32x16_bf16 v[68:83], v[228:231], v[132:135], v[68:83]
	ds_read_b128 v[224:227], v66 offset:32768
	ds_read_b128 v[228:231], v66 offset:49152
	v_add3_u32 v66, s6, v212, v200
	s_waitcnt lgkmcnt(1)
	v_mfma_f32_32x32x16_bf16 v[84:99], v[224:227], v[140:143], v[84:99]
	s_waitcnt lgkmcnt(0)
	v_mfma_f32_32x32x16_bf16 v[68:83], v[228:231], v[140:143], v[68:83]
	ds_read_b128 v[224:227], v66 offset:32768
	ds_read_b128 v[228:231], v66 offset:49152
	v_add3_u32 v66, s6, v213, v200
	s_waitcnt lgkmcnt(1)
	v_mfma_f32_32x32x16_bf16 v[84:99], v[224:227], v[136:139], v[84:99]
	s_waitcnt lgkmcnt(0)
	v_mfma_f32_32x32x16_bf16 v[68:83], v[228:231], v[136:139], v[68:83]
	ds_read_b128 v[224:227], v66 offset:32768
	ds_read_b128 v[228:231], v66 offset:49152
	s_waitcnt lgkmcnt(1)
	v_mfma_f32_32x32x16_bf16 v[84:99], v[224:227], v[144:147], v[84:99]
	s_waitcnt lgkmcnt(0)
	v_mfma_f32_32x32x16_bf16 v[68:83], v[228:231], v[144:147], v[68:83]
	s_setprio 0
	s_cmpk_eq_i32 s34, 0x41
	s_cbranch_scc1 .Lmv1_a
	s_cmp_gt_u32 s34, 60
	s_mov_b64 s[6:7], -1
	s_cbranch_scc0 .LBB0_895
	s_waitcnt vmcnt(0)
	s_mov_b64 s[6:7], 0

; DEV void partialSM(f32x16& p0, f32x16& p1, float& m_reg, float& mn, float& alpha) {
;   constexpr float C = SCALE * 1.4426950408889634f;
;   float pmax = p0[0];
; #pragma unroll
;   for (int r = 1; r < 16; ++r) pmax = fmaxf(pmax, p0[r]);
; #pragma unroll
;   for (int r = 0; r < 16; ++r) pmax = fmaxf(pmax, p1[r]);
;   { auto rr = __builtin_amdgcn_permlane32_swap(__float_as_uint(pmax), __float_as_uint(pmax), false, false);
;     pmax = fmaxf(__uint_as_float(rr[0]), __uint_as_float(rr[1])); }
;   if (__builtin_expect(__all(pmax - m_reg <= THR / SCALE), 1)) { mn = m_reg; alpha = 1.f; }
;   else { mn = fmaxf(m_reg, pmax); alpha = __builtin_amdgcn_exp2f((m_reg - mn) * C); m_reg = mn; }
.Lmv1_a:
	s_cmpk_gt_u32 s37, 0x41
	s_cbranch_scc1 .Lmv2_a
	v_add_co_u32_e32 v254, vcc, 0xffffe000, v188
	s_nop 1
	v_addc_co_u32_e32 v255, vcc, -1, v189, vcc
	global_load_dwordx4 v[148:151], v[254:255], off
	global_load_dwordx4 v[152:155], v[188:189], off
	v_add_co_u32_e32 v254, vcc, 0xffffc000, v190
	s_nop 1
	v_addc_co_u32_e32 v255, vcc, -1, v191, vcc
	global_load_dwordx4 v[156:159], v[254:255], off
	v_add_co_u32_e32 v254, vcc, 0xffffe000, v190
	s_nop 1
	v_addc_co_u32_e32 v255, vcc, -1, v191, vcc
	global_load_dwordx4 v[160:163], v[254:255], off
	global_load_dwordx4 v[164:167], v[190:191], off
.Lmv2_a:
	s_nop 8
	v_max_f32_e32 v66, v85, v85
	v_max_f32_e32 v219, v84, v84
	v_max_f32_e32 v66, v219, v66
	v_max3_f32 v66, v66, v86, v87
	v_max3_f32 v66, v66, v88, v89
	v_max3_f32 v66, v66, v90, v91
	v_max3_f32 v66, v66, v92, v93
	v_max3_f32 v66, v66, v94, v95
	v_max3_f32 v66, v66, v96, v97
	v_max3_f32 v66, v66, v98, v99
	v_max3_f32 v66, v66, v68, v69
	v_max3_f32 v66, v66, v70, v71
	v_max3_f32 v66, v66, v72, v73
	v_max3_f32 v66, v66, v74, v75
	v_max3_f32 v66, v66, v76, v77
	v_max3_f32 v66, v66, v78, v79
	v_max3_f32 v66, v66, v80, v81
	v_max3_f32 v66, v66, v82, v83
	v_mov_b32_e32 v219, v66
	s_nop 1
	v_permlane32_swap_b32_e32 v66, v219
	v_max_f32_e32 v219, v219, v219
	v_max_f32_e32 v66, v66, v66
	v_max_f32_e32 v66, v66, v219
	v_max_f32_e32 v220, v215, v215
	v_sub_f32_e32 v219, v66, v215
	v_max_f32_e32 v66, v220, v66
	v_sub_f32_e32 v220, v215, v66
	v_mul_f32_e32 v220, 0x3dd53b94, v220
	v_exp_f32_e32 v220, v220
	v_cmp_ge_f32_e32 vcc, s31, v219
	s_cmp_eq_u64 vcc, exec
	s_cselect_b64 s[6:7], -1, 0
	v_cndmask_b32_e64 v219, v220, 1.0, s[6:7]
	v_cmp_gt_f32_e32 vcc, 1.0, v219
	s_cbranch_vccz .LBB0_911
	s_and_saveexec_b64 s[24:25], s[4:5]
	ds_write_b32 v210, v219 offset:128
	s_or_b64 exec, exec, s[24:25]
	s_waitcnt lgkmcnt(0)
	v_add_u32_e32 v220, v185, v186
	ds_read_b128 v[224:227], v220 offset:224
	ds_read_b128 v[228:231], v220 offset:192
	ds_read_b128 v[232:235], v220 offset:160
	ds_read_b128 v[236:239], v220 offset:128
	s_waitcnt lgkmcnt(3)
	v_pk_mul_f32 v[62:63], v[62:63], v[224:225]
	s_waitcnt lgkmcnt(2)
	v_pk_mul_f32 v[58:59], v[58:59], v[228:229]
	s_waitcnt lgkmcnt(1)
	v_pk_mul_f32 v[54:55], v[54:55], v[232:233]
	v_pk_mul_f32 v[64:65], v[64:65], v[226:227]
	v_pk_mul_f32 v[60:61], v[60:61], v[230:231]
	v_pk_mul_f32 v[56:57], v[56:57], v[234:235]
	s_waitcnt lgkmcnt(0)
	v_pk_mul_f32 v[52:53], v[52:53], v[238:239]
	v_pk_mul_f32 v[50:51], v[50:51], v[236:237]
	v_pk_mul_f32 v[46:47], v[46:47], v[224:225]
	v_pk_mul_f32 v[42:43], v[42:43], v[228:229]
	v_pk_mul_f32 v[38:39], v[38:39], v[232:233]
	v_pk_mul_f32 v[48:49], v[48:49], v[226:227]
	v_pk_mul_f32 v[44:45], v[44:45], v[230:231]
	v_pk_mul_f32 v[40:41], v[40:41], v[234:235]
	v_pk_mul_f32 v[36:37], v[36:37], v[238:239]
	v_pk_mul_f32 v[34:35], v[34:35], v[236:237]
	v_pk_mul_f32 v[30:31], v[30:31], v[224:225]
	v_pk_mul_f32 v[26:27], v[26:27], v[228:229]
	v_pk_mul_f32 v[22:23], v[22:23], v[232:233]
	v_pk_mul_f32 v[32:33], v[32:33], v[226:227]
	v_pk_mul_f32 v[28:29], v[28:29], v[230:231]
	v_pk_mul_f32 v[24:25], v[24:25], v[234:235]
	v_pk_mul_f32 v[20:21], v[20:21], v[238:239]
	v_pk_mul_f32 v[18:19], v[18:19], v[236:237]
	v_pk_mul_f32 v[14:15], v[14:15], v[224:225]
	v_pk_mul_f32 v[10:11], v[10:11], v[228:229]
	v_pk_mul_f32 v[6:7], v[6:7], v[232:233]
	v_pk_mul_f32 v[16:17], v[16:17], v[226:227]
	v_pk_mul_f32 v[12:13], v[12:13], v[230:231]
	v_pk_mul_f32 v[8:9], v[8:9], v[234:235]
	v_pk_mul_f32 v[4:5], v[4:5], v[238:239]
	v_pk_mul_f32 v[2:3], v[2:3], v[236:237]

; #define SBAR() __builtin_amdgcn_sched_barrier(0)
; #define SLOAD(k0) do { vs0 = *reinterpret_cast<const bf16x8*>(Vh + (long)((k0) + sr) * DV + sc); vs1 = *reinterpret_cast<const bf16x8*>(Vh + (long)((k0) + 32 + sr) * DV + sc); \
;     const bf16_t* kp_ = Kh + (long)(k0) * QK + tid * 8; ks0 = *reinterpret_cast<const bf16x8*>(kp_); ks1 = *reinterpret_cast<const bf16x8*>(kp_ + 4096); ks2 = *reinterpret_cast<const bf16x8*>(kp_ + 8192); } while (0)
; #define SWRITE(b) do { *(bf16x8*)(V_lds + (b) * SHM_V + vst0) = vs0; *(bf16x8*)(V_lds + (b) * SHM_V + vst1) = vs1; \
;     *(bf16x8*)(K_lds + (b) * SHM_K + kst[0]) = ks0; *(bf16x8*)(K_lds + (b) * SHM_K + kst[1]) = ks1; *(bf16x8*)(K_lds + (b) * SHM_K + kst[2]) = ks2; } while (0)
; #define SWAIT() asm volatile("s_waitcnt vmcnt(0)" ::: "memory")
; DEV void attn_unit(const bf16_t* __restrict__ Qb, const bf16_t* __restrict__ Kh, const bf16_t* __restrict__ Vh, const float* __restrict__ rp, bf16_t* __restrict__ Ob, CParams& fp, int fwg, int fbase, int fn) {
;     ...
;   for (int j = 0; j < NTL; ++j) {
;     const int cb = j & 1;
;     if (j + 1 < NTL) { if (j >= 2 && j < fn) asm volatile("s_waitcnt vmcnt(5)" ::: "memory"); else SWAIT(); SWRITE(cb ^ 1); }
;     if (j + 2 < NTL) SLOAD((j + 2) * KVBLK);
;     if (j > 0 && j <= fn) fill_store(fp, fwg, fbase + j - 1, (j - 1) & 1);
;     SBAR(); qkt(p0, p1, K_lds + cb * SHM_K, qr, r32, hi);
.LBB0_1098:
.LBB0_1100:
.LBB0_1099:
	s_add_i32 s36, s35, 1
	s_cmp_gt_u32 s36, 61
	s_cbranch_scc0 .LBB0_1106
	s_branch .LBB0_1114

; #define SBAR() __builtin_amdgcn_sched_barrier(0)
; DEV void qkt(f32x16& p0, f32x16& p1, const char* Ks, const bf16x8* qr, int r32, int hi) {
;   p0 = f32x16{}; p1 = f32x16{};
;   __builtin_amdgcn_s_setprio(1);
; #pragma unroll
;   for (int d0 = 0; d0 < 12; ++d0) { const int cb = (d0 * 16 + hi * 8) * 2;
;     const bf16x8 b0 = *reinterpret_cast<const bf16x8*>(Ks + KSWZ2(r32, cb));
;     const bf16x8 b1 = *reinterpret_cast<const bf16x8*>(Ks + KSWZ2(32 + r32, cb));
;     p0 = __builtin_amdgcn_mfma_f32_32x32x16_bf16(b0, qr[d0], p0, 0, 0, 0);
;     p1 = __builtin_amdgcn_mfma_f32_32x32x16_bf16(b1, qr[d0], p1, 0, 0, 0); }
;   __builtin_amdgcn_s_setprio(0);
; }
; DEV void attn_unit(const bf16_t* __restrict__ Qb, const bf16_t* __restrict__ Kh, const bf16_t* __restrict__ Vh, const float* __restrict__ rp, bf16_t* __restrict__ Ob, CParams& fp, int fwg, int fbase, int fn) {
;     ...
;     SBAR(); qkt(p0, p1, K_lds + cb * SHM_K, qr, r32, hi);
.LBB0_1114:
	s_lshl_b32 s6, s37, 15
	s_add_i32 s6, s6, 0
	s_setprio 1
	v_add3_u32 v66, s6, v201, v200
	ds_read_b128 v[68:71], v66 offset:32768
	ds_read_b128 v[72:75], v66 offset:49152
	v_add3_u32 v66, s6, v202, v200
	ds_read_b128 v[224:227], v66 offset:32768
	ds_read_b128 v[228:231], v66 offset:49152
	v_add3_u32 v66, s6, v203, v200
	s_waitcnt lgkmcnt(0)
	v_mfma_f32_32x32x16_bf16 v[84:99], v[68:71], v[100:103], 0
	v_mfma_f32_32x32x16_bf16 v[68:83], v[72:75], v[100:103], 0
	v_mfma_f32_32x32x16_bf16 v[84:99], v[224:227], v[104:107], v[84:99]
	v_mfma_f32_32x32x16_bf16 v[68:83], v[228:231], v[104:107], v[68:83]
	ds_read_b128 v[224:227], v66 offset:32768
	ds_read_b128 v[228:231], v66 offset:49152
	v_add3_u32 v66, s6, v204, v200
	s_waitcnt lgkmcnt(1)
	v_mfma_f32_32x32x16_bf16 v[84:99], v[224:227], v[108:111], v[84:99]
	s_waitcnt lgkmcnt(0)
	v_mfma_f32_32x32x16_bf16 v[68:83], v[228:231], v[108:111], v[68:83]
	ds_read_b128 v[224:227], v66 offset:32768
	ds_read_b128 v[228:231], v66 offset:49152
	v_add3_u32 v66, s6, v205, v200
	s_waitcnt lgkmcnt(1)
	v_mfma_f32_32x32x16_bf16 v[84:99], v[224:227], v[112:115], v[84:99]
	s_waitcnt lgkmcnt(0)
	v_mfma_f32_32x32x16_bf16 v[68:83], v[228:231], v[112:115], v[68:83]
	ds_read_b128 v[224:227], v66 offset:32768
	ds_read_b128 v[228:231], v66 offset:49152
	v_add3_u32 v66, s6, v206, v200
	s_waitcnt lgkmcnt(1)
	v_mfma_f32_32x32x16_bf16 v[84:99], v[224:227], v[116:119], v[84:99]
	s_waitcnt lgkmcnt(0)
	v_mfma_f32_32x32x16_bf16 v[68:83], v[228:231], v[116:119], v[68:83]
	ds_read_b128 v[224:227], v66 offset:32768
	ds_read_b128 v[228:231], v66 offset:49152
	v_add3_u32 v66, s6, v207, v200
	s_waitcnt lgkmcnt(1)
	v_mfma_f32_32x32x16_bf16 v[84:99], v[224:227], v[120:123], v[84:99]
	s_waitcnt lgkmcnt(0)
	v_mfma_f32_32x32x16_bf16 v[68:83], v[228:231], v[120:123], v[68:83]
	ds_read_b128 v[224:227], v66 offset:32768
	ds_read_b128 v[228:231], v66 offset:49152
	v_add3_u32 v66, s6, v208, v200
	s_waitcnt lgkmcnt(1)
	v_mfma_f32_32x32x16_bf16 v[84:99], v[224:227], v[124:127], v[84:99]
	s_waitcnt lgkmcnt(0)
	v_mfma_f32_32x32x16_bf16 v[68:83], v[228:231], v[124:127], v[68:83]
	ds_read_b128 v[224:227], v66 offset:32768
	ds_read_b128 v[228:231], v66 offset:49152
	v_add3_u32 v66, s6, v209, v200
	s_waitcnt lgkmcnt(1)
	v_mfma_f32_32x32x16_bf16 v[84:99], v[224:227], v[128:131], v[84:99]
	s_waitcnt lgkmcnt(0)
	v_mfma_f32_32x32x16_bf16 v[68:83], v[228:231], v[128:131], v[68:83]
	ds_read_b128 v[224:227], v66 offset:32768
	ds_read_b128 v[228:231], v66 offset:49152
	v_add3_u32 v66, s6, v211, v200
	s_waitcnt lgkmcnt(1)
	v_mfma_f32_32x32x16_bf16 v[84:99], v[224:227], v[132:135], v[84:99]
	s_waitcnt lgkmcnt(0)
	v_mfma_f32_32x32x16_bf16 v[68:83], v[228:231], v[132:135], v[68:83]
	ds_read_b128 v[224:227], v66 offset:32768
	ds_read_b128 v[228:231], v66 offset:49152
	v_add3_u32 v66, s6, v212, v200
	s_waitcnt lgkmcnt(1)
	v_mfma_f32_32x32x16_bf16 v[84:99], v[224:227], v[140:143], v[84:99]
	s_waitcnt lgkmcnt(0)
	v_mfma_f32_32x32x16_bf16 v[68:83], v[228:231], v[140:143], v[68:83]
	ds_read_b128 v[224:227], v66 offset:32768
	ds_read_b128 v[228:231], v66 offset:49152
	v_add3_u32 v66, s6, v213, v200
	s_waitcnt lgkmcnt(1)
	v_mfma_f32_32x32x16_bf16 v[84:99], v[224:227], v[136:139], v[84:99]
	s_waitcnt lgkmcnt(0)
	v_mfma_f32_32x32x16_bf16 v[68:83], v[228:231], v[136:139], v[68:83]
	ds_read_b128 v[224:227], v66 offset:32768
	ds_read_b128 v[228:231], v66 offset:49152
	s_waitcnt lgkmcnt(1)
	v_mfma_f32_32x32x16_bf16 v[84:99], v[224:227], v[144:147], v[84:99]
	s_waitcnt lgkmcnt(0)
	v_mfma_f32_32x32x16_bf16 v[68:83], v[228:231], v[144:147], v[68:83]
	s_setprio 0
	s_cmpk_eq_i32 s35, 0x41
	s_cbranch_scc1 .Lmv1_b
	s_cmp_gt_u32 s35, 59
	s_mov_b64 s[6:7], -1
	s_cbranch_scc0 .LBB0_1102
	s_waitcnt vmcnt(0)
	s_mov_b64 s[6:7], 0

; DEV void partialSM(f32x16& p0, f32x16& p1, float& m_reg, float& mn, float& alpha) {
;   constexpr float C = SCALE * 1.4426950408889634f;
;   float pmax = p0[0];
; #pragma unroll
;   for (int r = 1; r < 16; ++r) pmax = fmaxf(pmax, p0[r]);
; #pragma unroll
;   for (int r = 0; r < 16; ++r) pmax = fmaxf(pmax, p1[r]);
;   { auto rr = __builtin_amdgcn_permlane32_swap(__float_as_uint(pmax), __float_as_uint(pmax), false, false);
;     pmax = fmaxf(__uint_as_float(rr[0]), __uint_as_float(rr[1])); }
;   if (__builtin_expect(__all(pmax - m_reg <= THR / SCALE), 1)) { mn = m_reg; alpha = 1.f; }
;   else { mn = fmaxf(m_reg, pmax); alpha = __builtin_amdgcn_exp2f((m_reg - mn) * C); m_reg = mn; }
.Lmv1_b:
	s_cmpk_gt_u32 s38, 0x41
	s_cbranch_scc1 .Lmv2_b
	v_add_co_u32_e32 v254, vcc, 0xffffe000, v188
	s_nop 1
	v_addc_co_u32_e32 v255, vcc, -1, v189, vcc
	global_load_dwordx4 v[148:151], v[254:255], off
	global_load_dwordx4 v[152:155], v[188:189], off
	v_add_co_u32_e32 v254, vcc, 0xffffc000, v190
	s_nop 1
	v_addc_co_u32_e32 v255, vcc, -1, v191, vcc
	global_load_dwordx4 v[156:159], v[254:255], off
	v_add_co_u32_e32 v254, vcc, 0xffffe000, v190
	s_nop 1
	v_addc_co_u32_e32 v255, vcc, -1, v191, vcc
	global_load_dwordx4 v[160:163], v[254:255], off
	global_load_dwordx4 v[164:167], v[190:191], off
.Lmv2_b:
	s_nop 8
	v_max_f32_e32 v66, v85, v85
	v_max_f32_e32 v219, v84, v84
	v_max_f32_e32 v66, v219, v66
	v_max3_f32 v66, v66, v86, v87
	v_max3_f32 v66, v66, v88, v89
	v_max3_f32 v66, v66, v90, v91
	v_max3_f32 v66, v66, v92, v93
	v_max3_f32 v66, v66, v94, v95
	v_max3_f32 v66, v66, v96, v97
	v_max3_f32 v66, v66, v98, v99
	v_max3_f32 v66, v66, v68, v69
	v_max3_f32 v66, v66, v70, v71
	v_max3_f32 v66, v66, v72, v73
	v_max3_f32 v66, v66, v74, v75
	v_max3_f32 v66, v66, v76, v77
	v_max3_f32 v66, v66, v78, v79
	v_max3_f32 v66, v66, v80, v81
	v_max3_f32 v66, v66, v82, v83
	v_mov_b32_e32 v219, v66
	s_nop 1
	v_permlane32_swap_b32_e32 v66, v219
	v_max_f32_e32 v219, v219, v219
	v_max_f32_e32 v66, v66, v66
	v_max_f32_e32 v66, v66, v219
	v_max_f32_e32 v220, v215, v215
	v_sub_f32_e32 v219, v66, v215
	v_max_f32_e32 v66, v220, v66
	v_sub_f32_e32 v220, v215, v66
	v_mul_f32_e32 v220, 0x3dd53b94, v220
	v_exp_f32_e32 v220, v220
	v_cmp_ge_f32_e32 vcc, s34, v219
	s_cmp_eq_u64 vcc, exec
	s_cselect_b64 s[6:7], -1, 0
	v_cndmask_b32_e64 v219, v220, 1.0, s[6:7]
	v_cmp_gt_f32_e32 vcc, 1.0, v219
	s_cbranch_vccz .LBB0_1118
	s_and_saveexec_b64 s[26:27], s[4:5]
	ds_write_b32 v210, v219 offset:128
	s_or_b64 exec, exec, s[26:27]
	s_waitcnt lgkmcnt(0)
	v_add_u32_e32 v220, v185, v186
	ds_read_b128 v[224:227], v220 offset:224
	ds_read_b128 v[228:231], v220 offset:192
	ds_read_b128 v[232:235], v220 offset:160
	ds_read_b128 v[236:239], v220 offset:128
	s_waitcnt lgkmcnt(3)
	v_pk_mul_f32 v[62:63], v[62:63], v[224:225]
	s_waitcnt lgkmcnt(2)
	v_pk_mul_f32 v[58:59], v[58:59], v[228:229]
	s_waitcnt lgkmcnt(1)
	v_pk_mul_f32 v[54:55], v[54:55], v[232:233]
	v_pk_mul_f32 v[64:65], v[64:65], v[226:227]
	v_pk_mul_f32 v[60:61], v[60:61], v[230:231]
	v_pk_mul_f32 v[56:57], v[56:57], v[234:235]
	s_waitcnt lgkmcnt(0)
	v_pk_mul_f32 v[52:53], v[52:53], v[238:239]
	v_pk_mul_f32 v[50:51], v[50:51], v[236:237]
	v_pk_mul_f32 v[46:47], v[46:47], v[224:225]
	v_pk_mul_f32 v[42:43], v[42:43], v[228:229]
	v_pk_mul_f32 v[38:39], v[38:39], v[232:233]
	v_pk_mul_f32 v[48:49], v[48:49], v[226:227]
	v_pk_mul_f32 v[44:45], v[44:45], v[230:231]
	v_pk_mul_f32 v[40:41], v[40:41], v[234:235]
	v_pk_mul_f32 v[36:37], v[36:37], v[238:239]
	v_pk_mul_f32 v[34:35], v[34:35], v[236:237]
	v_pk_mul_f32 v[30:31], v[30:31], v[224:225]
	v_pk_mul_f32 v[26:27], v[26:27], v[228:229]
	v_pk_mul_f32 v[22:23], v[22:23], v[232:233]
	v_pk_mul_f32 v[32:33], v[32:33], v[226:227]
	v_pk_mul_f32 v[28:29], v[28:29], v[230:231]
	v_pk_mul_f32 v[24:25], v[24:25], v[234:235]
	v_pk_mul_f32 v[20:21], v[20:21], v[238:239]
	v_pk_mul_f32 v[18:19], v[18:19], v[236:237]
	v_pk_mul_f32 v[14:15], v[14:15], v[224:225]
	v_pk_mul_f32 v[10:11], v[10:11], v[228:229]
	v_pk_mul_f32 v[6:7], v[6:7], v[232:233]
	v_pk_mul_f32 v[16:17], v[16:17], v[226:227]
	v_pk_mul_f32 v[12:13], v[12:13], v[230:231]
	v_pk_mul_f32 v[8:9], v[8:9], v[234:235]
	v_pk_mul_f32 v[4:5], v[4:5], v[238:239]
	v_pk_mul_f32 v[2:3], v[2:3], v[236:237]
